# baseline (speedup 1.0000x reference)
.LBB6_76:
	s_and_b32 s0, s14, 0x1ffc0
	v_pk_add_f16 v19, v28, v36
	v_or_b32_e32 v28, s0, v181
	v_pk_add_f16 v18, v29, v37
	v_lshlrev_b32_e32 v29, 8, v182
	v_lshlrev_b32_e32 v28, 14, v28
	v_pk_fma_f16 v23, v25, v37, v33
	v_rcp_f16_e32 v25, v18
	v_rcp_f16_sdwa v18, v18 dst_sel:DWORD dst_unused:UNUSED_PAD src0_sel:WORD_1
	v_or3_b32 v28, v29, v28, v180
	v_pk_add_f16 v17, v30, v38
	v_pk_fma_f16 v22, v24, v36, v32
	v_rcp_f16_e32 v24, v19
	v_rcp_f16_sdwa v19, v19 dst_sel:DWORD dst_unused:UNUSED_PAD src0_sel:WORD_1
	s_waitcnt lgkmcnt(0)
	s_and_b32 s13, s13, 0xffff
	s_mov_b32 s15, 0x20000
	s_mov_b32 s14, 0x800000
	v_lshlrev_b32_e32 v28, 1, v28
	s_waitcnt vmcnt(3)
	v_pk_add_f16 v15, v127, v15
	v_pk_add_f16 v14, v126, v14
	v_pk_add_f16 v13, v125, v13
	v_pk_add_f16 v12, v124, v12
	v_pk_add_f16 v16, v31, v39
	v_pk_fma_f16 v21, v26, v38, v34
	v_rcp_f16_e32 v26, v17
	v_rcp_f16_sdwa v17, v17 dst_sel:DWORD dst_unused:UNUSED_PAD src0_sel:WORD_1
	buffer_store_dwordx4 v[12:15], v28, s[12:15], 0 offen
	s_waitcnt vmcnt(3)
	v_pk_add_f16 v7, v91, v7
	v_pk_add_f16 v6, v90, v6
	v_or_b32_e32 v12, 0x8000, v28
	v_pk_add_f16 v5, v89, v5
	v_pk_add_f16 v4, v88, v4
	v_pk_fma_f16 v20, v27, v39, v35
	v_rcp_f16_e32 v27, v16
	v_rcp_f16_sdwa v16, v16 dst_sel:DWORD dst_unused:UNUSED_PAD src0_sel:WORD_1
	buffer_store_dwordx4 v[4:7], v12, s[12:15], 0 offen
	v_or_b32_e32 v12, 0x10000, v28
	s_waitcnt vmcnt(3)
	v_pk_add_f16 v7, v51, v11
	v_pk_add_f16 v6, v50, v10
	v_pk_add_f16 v5, v49, v9
	v_pk_add_f16 v4, v48, v8
	buffer_store_dwordx4 v[4:7], v12, s[12:15], 0 offen
	s_nop 1
	v_pack_b32_f16 v5, v25, v18
	s_waitcnt vmcnt(3)
	v_pk_fma_f16 v1, v23, v5, v1
	v_pack_b32_f16 v5, v24, v19
	v_pk_fma_f16 v0, v22, v5, v0
	v_pack_b32_f16 v5, v26, v17
	v_pk_fma_f16 v2, v21, v5, v2
	v_pack_b32_f16 v5, v27, v16
	v_or_b32_e32 v4, 0x18000, v28
	v_pk_fma_f16 v3, v20, v5, v3
	buffer_store_dwordx4 v[0:3], v4, s[12:15], 0 offen
	s_endpgm
